# speedup vs baseline: 1.0059x; 1.0059x over previous
.LBB2_11:
	s_add_i32 s33, s29, 0x2000
	s_cmpk_lg_i32 s29, 0x4000
	s_cselect_b32 s33, s33, 0
	v_add_u32_e32 v191, s31, v187
	ds_read_b64_tr_b16 v[148:149], v191 offset:24576
	ds_read_b64_tr_b16 v[150:151], v191 offset:25088
	v_mfma_f32_32x32x16_f16 v[64:79], v[56:59], v[124:127], v[32:47]
	v_exp_f32_e32 v88, v88
	v_exp_f32_e32 v89, v89
	v_cvt_pk_f16_f32 v140, v96, v97
	v_cvt_pk_f16_f32 v141, v98, v99
	ds_read_b64_tr_b16 v[144:145], v191 offset:28672
	ds_read_b64_tr_b16 v[146:147], v191 offset:29184
	v_mfma_f32_32x32x16_f16 v[48:63], v[176:179], v[124:127], v[32:47]
	v_exp_f32_e32 v90, v90
	v_exp_f32_e32 v91, v91
	v_pk_add_f16 v128, v140, v141
	v_cvt_pk_f16_f32 v142, v100, v101
	v_cvt_pk_f16_f32 v143, v102, v103
	ds_read_b64_tr_b16 v[96:97], v191 offset:25600
	ds_read_b64_tr_b16 v[98:99], v191 offset:26112
	v_mfma_f32_32x32x16_f16 v[64:79], v[172:175], v[120:123], v[64:79]
	v_exp_f32_e32 v92, v92
	v_exp_f32_e32 v93, v93
	v_pk_add_f16 v129, v142, v143
	v_cvt_pk_f16_f32 v136, v104, v105
	v_cvt_pk_f16_f32 v137, v106, v107
	ds_read_b64_tr_b16 v[100:101], v191 offset:29696
	ds_read_b64_tr_b16 v[102:103], v191 offset:30208
	v_mfma_f32_32x32x16_f16 v[48:63], v[168:171], v[120:123], v[48:63]
	v_exp_f32_e32 v94, v94
	v_exp_f32_e32 v95, v95
	v_pk_add_f16 v128, v128, v129
	v_cvt_pk_f16_f32 v138, v108, v109
	v_cvt_pk_f16_f32 v139, v110, v111
	v_pk_add_f16 v172, v136, v137
	s_min_u32 s31, s26, 27
	s_lshl_b32 s31, s31, 13
	s_add_u32 s31, s14, s31
	s_addc_u32 s35, s15, 0
	s_add_u32 s34, s31, 0x8000
	s_addc_u32 s35, s35, 0
	s_add_i32 s31, s29, s24
	s_mov_b32 s36, m0
	s_mov_b32 m0, s31
	s_nop 0
	global_load_lds_dwordx4 v189, s[34:35]
	s_mov_b32 m0, s36
	ds_read_b64_tr_b16 v[104:105], v191 offset:26624
	ds_read_b64_tr_b16 v[106:107], v191 offset:27136
	v_mfma_f32_32x32x16_f16 v[64:79], v[164:167], v[116:119], v[64:79]
	v_pk_add_f16 v108, v138, v139
	v_cvt_pk_f16_f32 v132, v80, v81
	v_cvt_pk_f16_f32 v133, v82, v83
	ds_read_b64_tr_b16 v[80:81], v191 offset:30720
	ds_read_b64_tr_b16 v[82:83], v191 offset:31232
	v_mfma_f32_32x32x16_f16 v[48:63], v[160:163], v[116:119], v[48:63]
	v_pk_add_f16 v129, v172, v108
	v_cvt_pk_f16_f32 v134, v84, v85
	v_cvt_pk_f16_f32 v135, v86, v87
	v_pk_add_f16 v164, v132, v133
	s_add_u32 s34, s27, 0x4000
	s_addc_u32 s35, s28, 0
	s_add_i32 s31, s33, s25
	s_mov_b32 s36, m0
	s_mov_b32 m0, s31
	s_nop 0
	global_load_lds_dwordx4 v189, s[34:35]
	s_mov_b32 m0, s36
	ds_read_b64_tr_b16 v[108:109], v191 offset:27648
	ds_read_b64_tr_b16 v[110:111], v191 offset:28160
	v_mfma_f32_32x32x16_f16 v[64:79], v[156:159], v[112:115], v[64:79]
	v_pk_add_f16 v161, v128, v129
	v_cvt_pk_f16_f32 v128, v88, v89
	v_cvt_pk_f16_f32 v129, v90, v91
	v_pk_add_f16 v160, v134, v135
	ds_read_b64_tr_b16 v[84:85], v191 offset:31744
	ds_read_b64_tr_b16 v[86:87], v191 offset:32256
	v_mfma_f32_32x32x16_f16 v[48:63], v[152:155], v[112:115], v[48:63]
	v_pk_add_f16 v88, v128, v129
	v_pk_add_f16 v89, v164, v160
	v_cvt_pk_f16_f32 v130, v92, v93
	v_cvt_pk_f16_f32 v131, v94, v95
	s_and_b64 vcc, exec, s[16:17]
	v_pk_add_f16 v89, v161, v89
	v_pk_add_f16 v90, v130, v131
	s_cbranch_vccnz .LBB2_13
	v_pk_add_f16 v91, v88, v90
	v_max3_f32 v93, v64, v65, v48
	v_max3_f32 v94, v66, v67, v49
	s_mov_b64 s[8:9], 0
	v_pk_add_f16 v91, v89, v91
	s_nop 0
	v_cvt_f32_f16_e32 v92, v91
	v_cvt_f32_f16_sdwa v91, v91 dst_sel:DWORD dst_unused:UNUSED_PAD src0_sel:WORD_1
	v_add_f32_e32 v91, v91, v92
	v_add_f32_e32 v188, v188, v91
	v_max3_f32 v91, v93, v50, v51
	v_max3_f32 v92, v94, v70, v71
	s_nop 0
	v_max3_f32 v91, v91, v68, v69
	v_max3_f32 v92, v92, v54, v55
	s_nop 0
	v_max3_f32 v91, v91, v52, v53
	v_max3_f32 v92, v92, v74, v75
	s_nop 0
	v_max3_f32 v91, v91, v72, v73
	v_max3_f32 v92, v92, v58, v59
	s_nop 0
	v_max3_f32 v91, v91, v56, v57
	v_max3_f32 v92, v92, v78, v79
	s_nop 0
	v_max3_f32 v91, v91, v76, v77
	v_max3_f32 v92, v92, v62, v63
	s_nop 0
	v_max3_f32 v91, v91, v60, v61
	s_nop 0
	v_max_f32 v91, v91, v92
	s_nop 0
	v_mov_b32_e32 v92, v91
	s_nop 1
	v_permlane32_swap_b32_e32 v91, v92
	v_max_f32 v91, v91, v92
	s_nop 0
	v_cmp_lt_f32_e32 vcc, s30, v91
	s_cbranch_vccnz .LBB2_22
